# router logits loop rewritten by hand: all 48 loads of an iteration in flight, rotating reloads, one counted vmcnt wait per 4-MFMA group
# speedup vs baseline: 1.0114x; 1.0038x over previous
; __device__ __forceinline__ void phase_router(const Params& p, LAS3 char* lds, int wid) {
;     ...
;             const float* hrow = p.h + (size_t)(t0 + n) * D + wid * 256 + 4 * kh;
;             const float* grow = p.ln_ffn_g + wid * 256 + 4 * kh;
;             const float* wrow = p.w_router + (size_t)(wid * 256 + 4 * kh) * 32 + n;
;             f32x16 acc;
; #pragma unroll
;             for (int r = 0; r < 16; ++r) acc[r] = 0.f;
;             float ssq = 0.f;
; #pragma unroll 1
;             for (int jj = 0; jj < 32; jj += 8) {
;                 f32x4 hv[8], gv[8];
; #pragma unroll
;                 for (int j = 0; j < 8; ++j) { hv[j] = *(const f32x4*)(hrow + 8 * (jj + j)); gv[j] = *(const f32x4*)(grow + 8 * (jj + j)); }
; #pragma unroll
;                 for (int j = 0; j < 8; ++j)
; #pragma unroll
;                     for (int i = 0; i < 4; ++i) {
;                         const float a = hv[j][i];
;                         ssq += a * a;
;                         const float bw = wrow[(size_t)(8 * (jj + j) + i) * 32];
;                         acc = __builtin_amdgcn_mfma_f32_32x32x2f32(a * gv[j][i], bw, acc, 0, 0, 0);
;                     }
;             }
.LBB0_338:
	v_lshl_add_u64 v[204:205], v[56:57], 0, v[48:49]
	v_lshl_add_u64 v[206:207], s[26:27], 0, v[48:49]
	global_load_dwordx4 v[106:109], v[204:205], off
	global_load_dwordx4 v[138:141], v[206:207], off
	global_load_dword v170, v[58:59], off offset:-4096
	global_load_dword v171, v[58:59], off offset:-3968
	global_load_dword v172, v[58:59], off offset:-3840
	global_load_dword v173, v[58:59], off offset:-3712
	global_load_dwordx4 v[110:113], v[204:205], off offset:32
	global_load_dwordx4 v[142:145], v[206:207], off offset:32
	global_load_dword v174, v[58:59], off offset:-3072
	global_load_dword v175, v[58:59], off offset:-2944
	global_load_dword v176, v[58:59], off offset:-2816
	global_load_dword v177, v[58:59], off offset:-2688
	global_load_dwordx4 v[114:117], v[204:205], off offset:64
	global_load_dwordx4 v[146:149], v[206:207], off offset:64
	global_load_dword v178, v[58:59], off offset:-2048
	global_load_dword v179, v[58:59], off offset:-1920
	global_load_dword v180, v[58:59], off offset:-1792
	global_load_dword v181, v[58:59], off offset:-1664
	global_load_dwordx4 v[118:121], v[204:205], off offset:96
	global_load_dwordx4 v[150:153], v[206:207], off offset:96
	global_load_dword v182, v[58:59], off offset:-1024
	global_load_dword v183, v[58:59], off offset:-896
	global_load_dword v184, v[58:59], off offset:-768
	global_load_dword v185, v[58:59], off offset:-640
	global_load_dwordx4 v[122:125], v[204:205], off offset:128
	global_load_dwordx4 v[154:157], v[206:207], off offset:128
	global_load_dword v186, v[58:59], off offset:0
	global_load_dword v187, v[58:59], off offset:128
	global_load_dword v188, v[58:59], off offset:256
	global_load_dword v189, v[58:59], off offset:384
	global_load_dwordx4 v[126:129], v[204:205], off offset:160
	global_load_dwordx4 v[158:161], v[206:207], off offset:160
	global_load_dword v190, v[58:59], off offset:1024
	global_load_dword v191, v[58:59], off offset:1152
	global_load_dword v192, v[58:59], off offset:1280
	global_load_dword v193, v[58:59], off offset:1408
	global_load_dwordx4 v[130:133], v[204:205], off offset:192
	global_load_dwordx4 v[162:165], v[206:207], off offset:192
	global_load_dword v194, v[58:59], off offset:2048
	global_load_dword v195, v[58:59], off offset:2176
	global_load_dword v196, v[58:59], off offset:2304
	global_load_dword v197, v[58:59], off offset:2432
	global_load_dwordx4 v[134:137], v[204:205], off offset:224
	global_load_dwordx4 v[166:169], v[206:207], off offset:224
	global_load_dword v198, v[58:59], off offset:3072
	global_load_dword v199, v[58:59], off offset:3200
	global_load_dword v200, v[58:59], off offset:3328
	global_load_dword v201, v[58:59], off offset:3456
	s_mov_b32 s11, 3
.Lrt_loop:
	v_lshl_add_u64 v[208:209], v[58:59], 0, s[12:13]
	s_waitcnt vmcnt(42)
	v_mul_f32_e32 v210, v106, v138
	v_mul_f32_e32 v211, v107, v139
	v_mul_f32_e32 v212, v108, v140
	v_mul_f32_e32 v213, v109, v141
	v_fmac_f32_e32 v51, v106, v106
	v_fmac_f32_e32 v51, v107, v107
	v_fmac_f32_e32 v51, v108, v108
	v_fmac_f32_e32 v51, v109, v109
	v_mfma_f32_32x32x2_f32 v[0:15], v210, v170, v[0:15]
	v_mfma_f32_32x32x2_f32 v[0:15], v211, v171, v[0:15]
	v_mfma_f32_32x32x2_f32 v[0:15], v212, v172, v[0:15]
	v_mfma_f32_32x32x2_f32 v[0:15], v213, v173, v[0:15]
	global_load_dwordx4 v[106:109], v[204:205], off offset:256
	global_load_dwordx4 v[138:141], v[206:207], off offset:256
	global_load_dword v170, v[208:209], off offset:-4096
	global_load_dword v171, v[208:209], off offset:-3968
	global_load_dword v172, v[208:209], off offset:-3840
	global_load_dword v173, v[208:209], off offset:-3712
	s_waitcnt vmcnt(42)
	v_mul_f32_e32 v210, v110, v142
	v_mul_f32_e32 v211, v111, v143
	v_mul_f32_e32 v212, v112, v144
	v_mul_f32_e32 v213, v113, v145
	v_fmac_f32_e32 v51, v110, v110
	v_fmac_f32_e32 v51, v111, v111
	v_fmac_f32_e32 v51, v112, v112
	v_fmac_f32_e32 v51, v113, v113
	v_mfma_f32_32x32x2_f32 v[0:15], v210, v174, v[0:15]
	v_mfma_f32_32x32x2_f32 v[0:15], v211, v175, v[0:15]
	v_mfma_f32_32x32x2_f32 v[0:15], v212, v176, v[0:15]
	v_mfma_f32_32x32x2_f32 v[0:15], v213, v177, v[0:15]
	global_load_dwordx4 v[110:113], v[204:205], off offset:288
	global_load_dwordx4 v[142:145], v[206:207], off offset:288
	global_load_dword v174, v[208:209], off offset:-3072
	global_load_dword v175, v[208:209], off offset:-2944
	global_load_dword v176, v[208:209], off offset:-2816
	global_load_dword v177, v[208:209], off offset:-2688
	s_waitcnt vmcnt(42)
	v_mul_f32_e32 v210, v114, v146
	v_mul_f32_e32 v211, v115, v147
	v_mul_f32_e32 v212, v116, v148
	v_mul_f32_e32 v213, v117, v149
	v_fmac_f32_e32 v51, v114, v114
	v_fmac_f32_e32 v51, v115, v115
	v_fmac_f32_e32 v51, v116, v116
	v_fmac_f32_e32 v51, v117, v117
	v_mfma_f32_32x32x2_f32 v[0:15], v210, v178, v[0:15]
	v_mfma_f32_32x32x2_f32 v[0:15], v211, v179, v[0:15]
	v_mfma_f32_32x32x2_f32 v[0:15], v212, v180, v[0:15]
	v_mfma_f32_32x32x2_f32 v[0:15], v213, v181, v[0:15]
	global_load_dwordx4 v[114:117], v[204:205], off offset:320
	global_load_dwordx4 v[146:149], v[206:207], off offset:320
	global_load_dword v178, v[208:209], off offset:-2048
	global_load_dword v179, v[208:209], off offset:-1920
	global_load_dword v180, v[208:209], off offset:-1792
	global_load_dword v181, v[208:209], off offset:-1664
	s_waitcnt vmcnt(42)
; __device__ __forceinline__ void phase_router(const Params& p, LAS3 char* lds, int wid) {
;     ...
;             for (int jj = 0; jj < 32; jj += 8) {
;                 f32x4 hv[8], gv[8];
; #pragma unroll
;                 for (int j = 0; j < 8; ++j) { hv[j] = *(const f32x4*)(hrow + 8 * (jj + j)); gv[j] = *(const f32x4*)(grow + 8 * (jj + j)); }
; #pragma unroll
;                 for (int j = 0; j < 8; ++j)
; #pragma unroll
;                     for (int i = 0; i < 4; ++i) {
;                         const float a = hv[j][i];
;                         ssq += a * a;
;                         const float bw = wrow[(size_t)(8 * (jj + j) + i) * 32];
;                         acc = __builtin_amdgcn_mfma_f32_32x32x2f32(a * gv[j][i], bw, acc, 0, 0, 0);
;                     }
;             }
	v_mul_f32_e32 v210, v118, v150
	v_mul_f32_e32 v211, v119, v151
	v_mul_f32_e32 v212, v120, v152
	v_mul_f32_e32 v213, v121, v153
	v_fmac_f32_e32 v51, v118, v118
	v_fmac_f32_e32 v51, v119, v119
	v_fmac_f32_e32 v51, v120, v120
	v_fmac_f32_e32 v51, v121, v121
	v_mfma_f32_32x32x2_f32 v[0:15], v210, v182, v[0:15]
	v_mfma_f32_32x32x2_f32 v[0:15], v211, v183, v[0:15]
	v_mfma_f32_32x32x2_f32 v[0:15], v212, v184, v[0:15]
	v_mfma_f32_32x32x2_f32 v[0:15], v213, v185, v[0:15]
	global_load_dwordx4 v[118:121], v[204:205], off offset:352
	global_load_dwordx4 v[150:153], v[206:207], off offset:352
	global_load_dword v182, v[208:209], off offset:-1024
	global_load_dword v183, v[208:209], off offset:-896
	global_load_dword v184, v[208:209], off offset:-768
	global_load_dword v185, v[208:209], off offset:-640
	s_waitcnt vmcnt(42)
	v_mul_f32_e32 v210, v122, v154
	v_mul_f32_e32 v211, v123, v155
	v_mul_f32_e32 v212, v124, v156
	v_mul_f32_e32 v213, v125, v157
	v_fmac_f32_e32 v51, v122, v122
	v_fmac_f32_e32 v51, v123, v123
	v_fmac_f32_e32 v51, v124, v124
	v_fmac_f32_e32 v51, v125, v125
	v_mfma_f32_32x32x2_f32 v[0:15], v210, v186, v[0:15]
	v_mfma_f32_32x32x2_f32 v[0:15], v211, v187, v[0:15]
	v_mfma_f32_32x32x2_f32 v[0:15], v212, v188, v[0:15]
	v_mfma_f32_32x32x2_f32 v[0:15], v213, v189, v[0:15]
	global_load_dwordx4 v[122:125], v[204:205], off offset:384
	global_load_dwordx4 v[154:157], v[206:207], off offset:384
	global_load_dword v186, v[208:209], off offset:0
	global_load_dword v187, v[208:209], off offset:128
	global_load_dword v188, v[208:209], off offset:256
	global_load_dword v189, v[208:209], off offset:384
	s_waitcnt vmcnt(42)
	v_mul_f32_e32 v210, v126, v158
	v_mul_f32_e32 v211, v127, v159
	v_mul_f32_e32 v212, v128, v160
	v_mul_f32_e32 v213, v129, v161
	v_fmac_f32_e32 v51, v126, v126
	v_fmac_f32_e32 v51, v127, v127
	v_fmac_f32_e32 v51, v128, v128
	v_fmac_f32_e32 v51, v129, v129
	v_mfma_f32_32x32x2_f32 v[0:15], v210, v190, v[0:15]
	v_mfma_f32_32x32x2_f32 v[0:15], v211, v191, v[0:15]
	v_mfma_f32_32x32x2_f32 v[0:15], v212, v192, v[0:15]
	v_mfma_f32_32x32x2_f32 v[0:15], v213, v193, v[0:15]
	global_load_dwordx4 v[126:129], v[204:205], off offset:416
	global_load_dwordx4 v[158:161], v[206:207], off offset:416
	global_load_dword v190, v[208:209], off offset:1024
	global_load_dword v191, v[208:209], off offset:1152
	global_load_dword v192, v[208:209], off offset:1280
	global_load_dword v193, v[208:209], off offset:1408
	s_waitcnt vmcnt(42)
	v_mul_f32_e32 v210, v130, v162
	v_mul_f32_e32 v211, v131, v163
	v_mul_f32_e32 v212, v132, v164
	v_mul_f32_e32 v213, v133, v165
	v_fmac_f32_e32 v51, v130, v130
	v_fmac_f32_e32 v51, v131, v131
	v_fmac_f32_e32 v51, v132, v132
	v_fmac_f32_e32 v51, v133, v133
	v_mfma_f32_32x32x2_f32 v[0:15], v210, v194, v[0:15]
	v_mfma_f32_32x32x2_f32 v[0:15], v211, v195, v[0:15]
	v_mfma_f32_32x32x2_f32 v[0:15], v212, v196, v[0:15]
	v_mfma_f32_32x32x2_f32 v[0:15], v213, v197, v[0:15]
	global_load_dwordx4 v[130:133], v[204:205], off offset:448
	global_load_dwordx4 v[162:165], v[206:207], off offset:448
	global_load_dword v194, v[208:209], off offset:2048
	global_load_dword v195, v[208:209], off offset:2176
	global_load_dword v196, v[208:209], off offset:2304
	global_load_dword v197, v[208:209], off offset:2432
	s_waitcnt vmcnt(42)
	v_mul_f32_e32 v210, v134, v166
	v_mul_f32_e32 v211, v135, v167
	v_mul_f32_e32 v212, v136, v168
	v_mul_f32_e32 v213, v137, v169
	v_fmac_f32_e32 v51, v134, v134
	v_fmac_f32_e32 v51, v135, v135
	v_fmac_f32_e32 v51, v136, v136
	v_fmac_f32_e32 v51, v137, v137
	v_mfma_f32_32x32x2_f32 v[0:15], v210, v198, v[0:15]
	v_mfma_f32_32x32x2_f32 v[0:15], v211, v199, v[0:15]
	v_mfma_f32_32x32x2_f32 v[0:15], v212, v200, v[0:15]
	v_mfma_f32_32x32x2_f32 v[0:15], v213, v201, v[0:15]
	global_load_dwordx4 v[134:137], v[204:205], off offset:480
	global_load_dwordx4 v[166:169], v[206:207], off offset:480
	global_load_dword v198, v[208:209], off offset:3072
	global_load_dword v199, v[208:209], off offset:3200
	global_load_dword v200, v[208:209], off offset:3328
	global_load_dword v201, v[208:209], off offset:3456
	v_lshl_add_u64 v[204:205], v[204:205], 0, s[14:15]
	v_lshl_add_u64 v[206:207], v[206:207], 0, s[14:15]
	v_mov_b64_e32 v[58:59], v[208:209]
	s_sub_u32 s11, s11, 1
	s_cmp_lg_u32 s11, 0
	s_cbranch_scc1 .Lrt_loop
; __device__ __forceinline__ float xor32(float v) { const int l = lane_id(); return __int_as_float(__builtin_amdgcn_ds_bpermute((l ^ 32) << 2, __float_as_int(v))); }
; __device__ __forceinline__ void phase_router(const Params& p, LAS3 char* lds, int wid) {
;     ...
;             for (int jj = 0; jj < 32; jj += 8) {
;                 f32x4 hv[8], gv[8];
; #pragma unroll
;                 for (int j = 0; j < 8; ++j) { hv[j] = *(const f32x4*)(hrow + 8 * (jj + j)); gv[j] = *(const f32x4*)(grow + 8 * (jj + j)); }
; #pragma unroll
;                 for (int j = 0; j < 8; ++j)
; #pragma unroll
;                     for (int i = 0; i < 4; ++i) {
;                         const float a = hv[j][i];
;                         ssq += a * a;
;                         const float bw = wrow[(size_t)(8 * (jj + j) + i) * 32];
;                         acc = __builtin_amdgcn_mfma_f32_32x32x2f32(a * gv[j][i], bw, acc, 0, 0, 0);
;                     }
;             }
;             ssq += xor32(ssq);
;             if (kh == 0) ssqp[wid * 32 + n] = ssq;
; #pragma unroll
;             for (int r = 0; r < 16; ++r) part[(wid * 32 + ((r & 3) + 8 * (r >> 2) + 4 * kh)) * 33 + n] = acc[r];
	s_waitcnt vmcnt(42)
	v_mul_f32_e32 v210, v106, v138
	v_mul_f32_e32 v211, v107, v139
	v_mul_f32_e32 v212, v108, v140
	v_mul_f32_e32 v213, v109, v141
	v_fmac_f32_e32 v51, v106, v106
	v_fmac_f32_e32 v51, v107, v107
	v_fmac_f32_e32 v51, v108, v108
	v_fmac_f32_e32 v51, v109, v109
	v_mfma_f32_32x32x2_f32 v[0:15], v210, v170, v[0:15]
	v_mfma_f32_32x32x2_f32 v[0:15], v211, v171, v[0:15]
	v_mfma_f32_32x32x2_f32 v[0:15], v212, v172, v[0:15]
	v_mfma_f32_32x32x2_f32 v[0:15], v213, v173, v[0:15]
	s_waitcnt vmcnt(36)
	v_mul_f32_e32 v210, v110, v142
	v_mul_f32_e32 v211, v111, v143
	v_mul_f32_e32 v212, v112, v144
	v_mul_f32_e32 v213, v113, v145
	v_fmac_f32_e32 v51, v110, v110
	v_fmac_f32_e32 v51, v111, v111
	v_fmac_f32_e32 v51, v112, v112
	v_fmac_f32_e32 v51, v113, v113
	v_mfma_f32_32x32x2_f32 v[0:15], v210, v174, v[0:15]
	v_mfma_f32_32x32x2_f32 v[0:15], v211, v175, v[0:15]
	v_mfma_f32_32x32x2_f32 v[0:15], v212, v176, v[0:15]
	v_mfma_f32_32x32x2_f32 v[0:15], v213, v177, v[0:15]
	s_waitcnt vmcnt(30)
	v_mul_f32_e32 v210, v114, v146
	v_mul_f32_e32 v211, v115, v147
	v_mul_f32_e32 v212, v116, v148
	v_mul_f32_e32 v213, v117, v149
	v_fmac_f32_e32 v51, v114, v114
	v_fmac_f32_e32 v51, v115, v115
	v_fmac_f32_e32 v51, v116, v116
	v_fmac_f32_e32 v51, v117, v117
	v_mfma_f32_32x32x2_f32 v[0:15], v210, v178, v[0:15]
	v_mfma_f32_32x32x2_f32 v[0:15], v211, v179, v[0:15]
	v_mfma_f32_32x32x2_f32 v[0:15], v212, v180, v[0:15]
	v_mfma_f32_32x32x2_f32 v[0:15], v213, v181, v[0:15]
	s_waitcnt vmcnt(24)
	v_mul_f32_e32 v210, v118, v150
	v_mul_f32_e32 v211, v119, v151
	v_mul_f32_e32 v212, v120, v152
	v_mul_f32_e32 v213, v121, v153
	v_fmac_f32_e32 v51, v118, v118
	v_fmac_f32_e32 v51, v119, v119
	v_fmac_f32_e32 v51, v120, v120
	v_fmac_f32_e32 v51, v121, v121
	v_mfma_f32_32x32x2_f32 v[0:15], v210, v182, v[0:15]
	v_mfma_f32_32x32x2_f32 v[0:15], v211, v183, v[0:15]
	v_mfma_f32_32x32x2_f32 v[0:15], v212, v184, v[0:15]
	v_mfma_f32_32x32x2_f32 v[0:15], v213, v185, v[0:15]
	s_waitcnt vmcnt(18)
	v_mul_f32_e32 v210, v122, v154
	v_mul_f32_e32 v211, v123, v155
	v_mul_f32_e32 v212, v124, v156
	v_mul_f32_e32 v213, v125, v157
	v_fmac_f32_e32 v51, v122, v122
	v_fmac_f32_e32 v51, v123, v123
	v_fmac_f32_e32 v51, v124, v124
	v_fmac_f32_e32 v51, v125, v125
	v_mfma_f32_32x32x2_f32 v[0:15], v210, v186, v[0:15]
	v_mfma_f32_32x32x2_f32 v[0:15], v211, v187, v[0:15]
	v_mfma_f32_32x32x2_f32 v[0:15], v212, v188, v[0:15]
	v_mfma_f32_32x32x2_f32 v[0:15], v213, v189, v[0:15]
	s_waitcnt vmcnt(12)
	v_mul_f32_e32 v210, v126, v158
	v_mul_f32_e32 v211, v127, v159
	v_mul_f32_e32 v212, v128, v160
	v_mul_f32_e32 v213, v129, v161
	v_fmac_f32_e32 v51, v126, v126
	v_fmac_f32_e32 v51, v127, v127
	v_fmac_f32_e32 v51, v128, v128
	v_fmac_f32_e32 v51, v129, v129
	v_mfma_f32_32x32x2_f32 v[0:15], v210, v190, v[0:15]
	v_mfma_f32_32x32x2_f32 v[0:15], v211, v191, v[0:15]
	v_mfma_f32_32x32x2_f32 v[0:15], v212, v192, v[0:15]
	v_mfma_f32_32x32x2_f32 v[0:15], v213, v193, v[0:15]
	s_waitcnt vmcnt(6)
	v_mul_f32_e32 v210, v130, v162
	v_mul_f32_e32 v211, v131, v163
	v_mul_f32_e32 v212, v132, v164
	v_mul_f32_e32 v213, v133, v165
	v_fmac_f32_e32 v51, v130, v130
	v_fmac_f32_e32 v51, v131, v131
	v_fmac_f32_e32 v51, v132, v132
	v_fmac_f32_e32 v51, v133, v133
	v_mfma_f32_32x32x2_f32 v[0:15], v210, v194, v[0:15]
	v_mfma_f32_32x32x2_f32 v[0:15], v211, v195, v[0:15]
	v_mfma_f32_32x32x2_f32 v[0:15], v212, v196, v[0:15]
	v_mfma_f32_32x32x2_f32 v[0:15], v213, v197, v[0:15]
	s_waitcnt vmcnt(0)
	v_mul_f32_e32 v210, v134, v166
	v_mul_f32_e32 v211, v135, v167
	v_mul_f32_e32 v212, v136, v168
	v_mul_f32_e32 v213, v137, v169
	v_fmac_f32_e32 v51, v134, v134
	v_fmac_f32_e32 v51, v135, v135
	v_fmac_f32_e32 v51, v136, v136
	v_fmac_f32_e32 v51, v137, v137
	v_mfma_f32_32x32x2_f32 v[0:15], v210, v198, v[0:15]
	v_mfma_f32_32x32x2_f32 v[0:15], v211, v199, v[0:15]
	v_mfma_f32_32x32x2_f32 v[0:15], v212, v200, v[0:15]
	v_mfma_f32_32x32x2_f32 v[0:15], v213, v201, v[0:15]
	v_mbcnt_lo_u32_b32 v16, -1, 0
	v_mbcnt_hi_u32_b32 v16, -1, v16
	s_nop 0
	v_lshlrev_b32_e32 v16, 2, v16
	v_xor_b32_e32 v16, 0x80, v16
	ds_bpermute_b32 v16, v16, v51
	s_and_saveexec_b64 s[26:27], s[4:5]
	s_cbranch_execz .LBB0_341
	s_waitcnt lgkmcnt(0)
	v_add_f32_e32 v16, v51, v16
	v_add_u32_e32 v17, s2, v60
	ds_write_b32 v17, v16 offset:34816
